# half-chip phase staggering: groups 4-7 start R2(L0) only after groups 0-3 finished theirs (spin on the existing QKV gate counter); on top of spare-XCD conversion
# baseline (speedup 1.0000x reference)
; #define KIN(i) ((const float*)(GAS const float*)karg()[i])
; #define KOUT() ((float*)(GAS float*)karg()[19])
; #define WSP(type, off) ((type*)(KWS() + (off)))
; #define IDS() const int lane = lane_id(), tid = wave * 64 + lane; (void)tid; (void)lane
; #define CBID() (LOCAL_OK() ? ((bid & 7) * 32 + (bid >> 3)) : bid)
; #define MODL() (WSP(float, WS_MOD) + (size_t)l * 16 * 6144)
; #define MODL() (WSP(float, WS_MOD) + (size_t)l * 16 * 6144)
;     __device__ __forceinline__ void gate_wait() const {
;         unsigned sp = 0u;
;         while (__hip_atomic_load(gate, __ATOMIC_RELAXED, __HIP_MEMORY_SCOPE_AGENT) < want) { __builtin_amdgcn_s_sleep(2); if (++sp > (1u << 22)) break; }
;     }
; __global__ void __launch_bounds__(NWAVES * 64, 2) mk_fwd(Args args) {
;     ...
;         for (int rep_ = 0; rep_ < REPS(8); ++rep_) if (IN(pb0 + 3)) { IDS(); const bool dry = rep_ + 1 < REPS(8);
;             const float* gnext = (l == 0) ? KIN(2) + D : KIN(18);
;             const float* modn = WSP(float, WS_MOD) + (size_t)16 * 6144; const float* modl = MODL();
;             float* outf = KOUT(); bf16_t* xr = (bf16_t*)KOUT(); const bf16_t* yw = WSP(bf16_t, WS_YW); const int* tslot = WSP(int, WS_TSLOT); bf16_t* xn = WSP(bf16_t, WS_XN);
;             for (int w0 = (CBID() * 8 + wave) * 32; w0 < T; w0 += G * 8 * 32) {
.LBB0_1714:
	s_bitcmp1_b32 s83, 2
	s_cbranch_scc0 .Lr2g_go
	v_readlane_b32 s98, v251, 25
	v_readlane_b32 s99, v251, 26
	s_nop 4
	s_load_dwordx2 s[98:99], s[98:99], 0xa0
	v_mov_b32_e32 v252, 0
	s_waitcnt lgkmcnt(0)
	s_add_u32 s98, s98, 0x9400
	s_addc_u32 s99, s99, 0
.Lr2g_spin:
	global_load_dword v253, v252, s[98:99] sc1
	s_waitcnt vmcnt(0)
	v_readfirstlane_b32 s100, v253
	s_nop 1
	s_cmp_ge_u32 s100, 0x80
	s_cbranch_scc1 .Lr2g_go
	s_sleep 8
	s_branch .Lr2g_spin
